# c29: c23 + attention tile loops: packed f32 sub/sum (v_pk_add_f32), folded LDS address adds into ds offsets
# speedup vs baseline: 1.0068x; 1.0068x over previous
; #define LAS __attribute__((address_space(3)))
; template <bool BAND, int OUTMODE>
; __device__ __forceinline__ void compute(LAS unsigned char* lds, const bf16x8 (&qr)[4], int tid, int mq0, int dil, int res, int kt_min, int bias_tab, float sink2,
;                                         bf16* ob, int opitch, float* lsep) {
;     ...
;             for (int i = 0; i < 16; ++i) S[i] = bl[32 * t + (i & 3) + 8 * (i >> 2)];
;         } else {
; #pragma unroll
;             for (int i = 0; i < 16; ++i) S[i] = 0.f;
;         }
; #pragma unroll
;         for (int s = 0; s < 4; ++s) { const bf16x8 kf = *(const LAS bf16x8*)(kb + t * 32 * KSTR + s * 32); S = __builtin_amdgcn_mfma_f32_32x32x16_bf16(kf, qr[s], S, 0, 0, 0); }
;         float m0 = fmaxf(fmaxf(S[0], S[1]), fmaxf(S[2], S[3])), m1 = fmaxf(fmaxf(S[4], S[5]), fmaxf(S[6], S[7])), m2 = fmaxf(fmaxf(S[8], S[9]), fmaxf(S[10], S[11])), m3 = fmaxf(fmaxf(S[12], S[13]), fmaxf(S[14], S[15]));
;         const float mt = xhalf_max(fmaxf(fmaxf(m0, m1), fmaxf(m2, m3)));
;         if (__any(mt > mref + THR)) {
;             const float mnew = fmaxf(mref, mt), f = __builtin_amdgcn_exp2f(mref - mnew);
;             mref = mnew; l *= f;
; #pragma unroll
;             for (int i = 0; i < 16; ++i) { o0[i] *= f; o1[i] *= f; }
;         }
; #pragma unroll
;         for (int i = 0; i < 16; ++i) { const float p = __builtin_amdgcn_exp2f(S[i] - mref); S[i] = p; l += p; }
; #pragma unroll
;         for (int s = 0; s < 2; ++s) {
;             v4u pw; pw.x = cvtpk(S[8 * s + 0], S[8 * s + 1]); pw.y = cvtpk(S[8 * s + 2], S[8 * s + 3]); pw.z = cvtpk(S[8 * s + 4], S[8 * s + 5]); pw.w = cvtpk(S[8 * s + 6], S[8 * s + 7]);
;             const bf16x8 pa = __builtin_bit_cast(bf16x8, pw);
;             const LAS unsigned char* vp = vb + (32 * t + 16 * s) * 64;
;             const s16x4 a0 = vtr(vp), a1 = vtr(vp + 8 * 64), b0 = vtr(vp + VPLANE), b1 = vtr(vp + VPLANE + 8 * 64);
;             const bf16x8 v0 = __builtin_shufflevector(a0, a1, 0, 1, 2, 3, 4, 5, 6, 7), v1 = __builtin_shufflevector(b0, b1, 0, 1, 2, 3, 4, 5, 6, 7);
;             o0 = __builtin_amdgcn_mfma_f32_32x32x16_bf16(v0, pa, o0, 0, 0, 0);
;             o1 = __builtin_amdgcn_mfma_f32_32x32x16_bf16(v1, pa, o1, 0, 0, 0);
;         }
;     }
.LBB0_371:
	v_pk_add_f32 v[220:221], v[36:37], v[166:167] op_sel:[0,1] op_sel_hi:[1,1] neg_lo:[0,1] neg_hi:[0,1]
	v_pk_add_f32 v[222:223], v[38:39], v[166:167] op_sel:[0,1] op_sel_hi:[1,1] neg_lo:[0,1] neg_hi:[0,1]
	v_pk_add_f32 v[224:225], v[40:41], v[166:167] op_sel:[0,1] op_sel_hi:[1,1] neg_lo:[0,1] neg_hi:[0,1]
	v_pk_add_f32 v[226:227], v[42:43], v[166:167] op_sel:[0,1] op_sel_hi:[1,1] neg_lo:[0,1] neg_hi:[0,1]
	v_pk_add_f32 v[228:229], v[44:45], v[166:167] op_sel:[0,1] op_sel_hi:[1,1] neg_lo:[0,1] neg_hi:[0,1]
	v_pk_add_f32 v[230:231], v[46:47], v[166:167] op_sel:[0,1] op_sel_hi:[1,1] neg_lo:[0,1] neg_hi:[0,1]
	v_pk_add_f32 v[232:233], v[48:49], v[166:167] op_sel:[0,1] op_sel_hi:[1,1] neg_lo:[0,1] neg_hi:[0,1]
	v_pk_add_f32 v[234:235], v[50:51], v[166:167] op_sel:[0,1] op_sel_hi:[1,1] neg_lo:[0,1] neg_hi:[0,1]
	v_exp_f32_e32 v200, v220
	v_exp_f32_e32 v201, v221
	v_exp_f32_e32 v202, v222
	v_exp_f32_e32 v203, v223
	v_exp_f32_e32 v204, v224
	v_exp_f32_e32 v205, v225
	v_exp_f32_e32 v206, v226
	v_exp_f32_e32 v207, v227
	v_add_u32_e32 v184, 0, v159
	v_exp_f32_e32 v208, v228
	ds_read_b64_tr_b16 v[40:41], v184 offset:55296
	ds_read_b64_tr_b16 v[42:43], v184 offset:55808
	v_exp_f32_e32 v209, v229
	v_add_u32_e32 v245, 0x6000, v184
	v_exp_f32_e32 v210, v230
	ds_read_b64_tr_b16 v[44:45], v245 offset:55296
	ds_read_b64_tr_b16 v[46:47], v245 offset:55808
	ds_read_b64_tr_b16 v[168:169], v184 offset:56320
	ds_read_b64_tr_b16 v[170:171], v184 offset:56832
	v_exp_f32_e32 v211, v231
	v_exp_f32_e32 v212, v232
	v_cvt_pk_bf16_f32 v36, v200, v201
	v_cvt_pk_bf16_f32 v37, v202, v203
	v_cvt_pk_bf16_f32 v38, v204, v205
	v_cvt_pk_bf16_f32 v39, v206, v207
	s_add_i32 s18, s18, 1
	s_waitcnt lgkmcnt(4)
	v_mfma_f32_32x32x16_bf16 v[20:35], v[40:43], v[36:39], v[20:35]
	v_exp_f32_e32 v213, v233
	ds_read_b64_tr_b16 v[40:41], v245 offset:56320
	ds_read_b64_tr_b16 v[42:43], v245 offset:56832
	v_add_u32_e32 v159, 0x800, v159
	v_add_u32_e32 v161, 0x1200, v161
	s_waitcnt lgkmcnt(4)
	v_mfma_f32_32x32x16_bf16 v[4:19], v[44:47], v[36:39], v[4:19]
	v_exp_f32_e32 v214, v234
	v_exp_f32_e32 v215, v235
	v_cvt_pk_bf16_f32 v36, v208, v209
	v_cvt_pk_bf16_f32 v37, v210, v211
	v_cvt_pk_bf16_f32 v38, v212, v213
	v_cvt_pk_bf16_f32 v39, v214, v215
	s_cmp_lt_u32 s18, 4
	v_add_u32_e32 v166, 0x80, v166
	s_waitcnt lgkmcnt(2)
	v_mfma_f32_32x32x16_bf16 v[20:35], v[168:171], v[36:39], v[20:35]
	s_waitcnt lgkmcnt(0)
	v_mfma_f32_32x32x16_bf16 v[4:19], v[40:43], v[36:39], v[4:19]
	v_pk_add_f32 v[236:237], v[200:201], v[202:203]
	v_pk_add_f32 v[238:239], v[204:205], v[206:207]
	v_pk_add_f32 v[240:241], v[208:209], v[210:211]
	v_pk_add_f32 v[242:243], v[212:213], v[214:215]
	v_pk_add_f32 v[236:237], v[236:237], v[238:239]
	v_pk_add_f32 v[240:241], v[240:241], v[242:243]
	v_pk_add_f32 v[236:237], v[236:237], v[240:241]
	v_add_f32_e32 v236, v236, v237
	v_add_f32_e32 v137, v137, v236
	s_cbranch_scc0 .LBB0_374
.LBB0_372:
	v_add_u32_e32 v244, 0x19800, v166
	ds_read2_b32 v[36:37], v244 offset1:1
	ds_read2_b32 v[38:39], v244 offset0:2 offset1:3
	ds_read2_b32 v[40:41], v244 offset0:8 offset1:9
	ds_read2_b32 v[42:43], v244 offset0:10 offset1:11
	v_add_u32_e32 v176, 0, v161
	ds_read_b128 v[168:171], v176
	ds_read2_b32 v[44:45], v244 offset0:16 offset1:17
	ds_read2_b32 v[46:47], v244 offset0:18 offset1:19
	ds_read2_b32 v[48:49], v244 offset0:24 offset1:25
	ds_read2_b32 v[50:51], v244 offset0:26 offset1:27
	ds_read_b128 v[172:175], v176 offset:32
	s_waitcnt vmcnt(18) lgkmcnt(1)
	v_mfma_f32_32x32x16_bf16 v[36:51], v[168:171], v[118:121], v[36:51]
	s_waitcnt vmcnt(17) lgkmcnt(0)
	v_mfma_f32_32x32x16_bf16 v[36:51], v[172:175], v[122:125], v[36:51]
	ds_read_b128 v[168:171], v176 offset:64
	ds_read_b128 v[172:175], v176 offset:96
	s_waitcnt vmcnt(16) lgkmcnt(1)
	v_mfma_f32_32x32x16_bf16 v[36:51], v[168:171], v[126:129], v[36:51]
	s_waitcnt vmcnt(15) lgkmcnt(0)
	v_mfma_f32_32x32x16_bf16 v[36:51], v[172:175], v[130:133], v[36:51]
	s_nop 11
	v_max3_f32 v168, v36, v37, v38
	v_max3_f32 v169, v39, v40, v41
	v_max3_f32 v170, v42, v43, v44
	v_max3_f32 v171, v45, v46, v47
	v_max3_f32 v172, v48, v49, v50
	v_max3_f32 v168, v168, v169, v51
	v_max3_f32 v170, v170, v171, v172
	v_max_f32_e32 v168, v168, v170
	v_mov_b32_e32 v169, v168
	s_nop 1
	v_permlane32_swap_b32_e32 v168, v169
	v_max_f32_e32 v168, v168, v169
	v_add_f32_e32 v169, 0x41000000, v167
	v_cmp_gt_f32_e32 vcc, v168, v169
	s_cbranch_vccz .LBB0_371
	v_max_f32_e32 v168, v168, v168
	v_max_f32_e32 v169, v167, v167
	v_max_f32_e32 v169, v169, v168
	v_sub_f32_e32 v167, v167, v169
	v_exp_f32_e32 v168, v167
	v_mov_b32_e32 v167, v169
	v_pk_mul_f32 v[34:35], v[34:35], v[168:169] op_sel_hi:[1,0]
	v_pk_mul_f32 v[32:33], v[32:33], v[168:169] op_sel_hi:[1,0]
	v_pk_mul_f32 v[30:31], v[30:31], v[168:169] op_sel_hi:[1,0]
	v_pk_mul_f32 v[28:29], v[28:29], v[168:169] op_sel_hi:[1,0]
	v_pk_mul_f32 v[26:27], v[26:27], v[168:169] op_sel_hi:[1,0]
	v_pk_mul_f32 v[24:25], v[24:25], v[168:169] op_sel_hi:[1,0]
	v_pk_mul_f32 v[22:23], v[22:23], v[168:169] op_sel_hi:[1,0]
	v_pk_mul_f32 v[20:21], v[20:21], v[168:169] op_sel_hi:[1,0]
	v_pk_mul_f32 v[18:19], v[18:19], v[168:169] op_sel_hi:[1,0]
	v_pk_mul_f32 v[16:17], v[16:17], v[168:169] op_sel_hi:[1,0]
	v_pk_mul_f32 v[14:15], v[14:15], v[168:169] op_sel_hi:[1,0]
	v_pk_mul_f32 v[12:13], v[12:13], v[168:169] op_sel_hi:[1,0]
	v_pk_mul_f32 v[10:11], v[10:11], v[168:169] op_sel_hi:[1,0]
	v_pk_mul_f32 v[8:9], v[8:9], v[168:169] op_sel_hi:[1,0]
	v_pk_mul_f32 v[6:7], v[6:7], v[168:169] op_sel_hi:[1,0]
	v_pk_mul_f32 v[4:5], v[4:5], v[168:169] op_sel_hi:[1,0]
	v_mul_f32_e32 v137, v137, v168
	s_branch .LBB0_371

; #define LAS __attribute__((address_space(3)))
; template <bool BAND, int OUTMODE>
; __device__ __forceinline__ void compute(LAS unsigned char* lds, const bf16x8 (&qr)[4], int tid, int mq0, int dil, int res, int kt_min, int bias_tab, float sink2,
;                                         bf16* ob, int opitch, float* lsep) {
;     ...
;             for (int i = 0; i < 16; ++i) S[i] = bl[32 * t + (i & 3) + 8 * (i >> 2)];
;         } else {
; #pragma unroll
;             for (int i = 0; i < 16; ++i) S[i] = 0.f;
;         }
; #pragma unroll
;         for (int s = 0; s < 4; ++s) { const bf16x8 kf = *(const LAS bf16x8*)(kb + t * 32 * KSTR + s * 32); S = __builtin_amdgcn_mfma_f32_32x32x16_bf16(kf, qr[s], S, 0, 0, 0); }
;         float m0 = fmaxf(fmaxf(S[0], S[1]), fmaxf(S[2], S[3])), m1 = fmaxf(fmaxf(S[4], S[5]), fmaxf(S[6], S[7])), m2 = fmaxf(fmaxf(S[8], S[9]), fmaxf(S[10], S[11])), m3 = fmaxf(fmaxf(S[12], S[13]), fmaxf(S[14], S[15]));
;         const float mt = xhalf_max(fmaxf(fmaxf(m0, m1), fmaxf(m2, m3)));
;         if (__any(mt > mref + THR)) {
;             const float mnew = fmaxf(mref, mt), f = __builtin_amdgcn_exp2f(mref - mnew);
;             mref = mnew; l *= f;
; #pragma unroll
;             for (int i = 0; i < 16; ++i) { o0[i] *= f; o1[i] *= f; }
;         }
; #pragma unroll
;         for (int i = 0; i < 16; ++i) { const float p = __builtin_amdgcn_exp2f(S[i] - mref); S[i] = p; l += p; }
; #pragma unroll
;         for (int s = 0; s < 2; ++s) {
;             v4u pw; pw.x = cvtpk(S[8 * s + 0], S[8 * s + 1]); pw.y = cvtpk(S[8 * s + 2], S[8 * s + 3]); pw.z = cvtpk(S[8 * s + 4], S[8 * s + 5]); pw.w = cvtpk(S[8 * s + 6], S[8 * s + 7]);
;             const bf16x8 pa = __builtin_bit_cast(bf16x8, pw);
;             const LAS unsigned char* vp = vb + (32 * t + 16 * s) * 64;
;             const s16x4 a0 = vtr(vp), a1 = vtr(vp + 8 * 64), b0 = vtr(vp + VPLANE), b1 = vtr(vp + VPLANE + 8 * 64);
;             const bf16x8 v0 = __builtin_shufflevector(a0, a1, 0, 1, 2, 3, 4, 5, 6, 7), v1 = __builtin_shufflevector(b0, b1, 0, 1, 2, 3, 4, 5, 6, 7);
;             o0 = __builtin_amdgcn_mfma_f32_32x32x16_bf16(v0, pa, o0, 0, 0, 0);
;             o1 = __builtin_amdgcn_mfma_f32_32x32x16_bf16(v1, pa, o1, 0, 0, 0);
;         }
;     }
.LBB0_379:
	v_pk_add_f32 v[220:221], v[36:37], v[138:139] op_sel:[0,1] op_sel_hi:[1,1] neg_lo:[0,1] neg_hi:[0,1]
	v_pk_add_f32 v[222:223], v[38:39], v[138:139] op_sel:[0,1] op_sel_hi:[1,1] neg_lo:[0,1] neg_hi:[0,1]
	v_pk_add_f32 v[224:225], v[40:41], v[138:139] op_sel:[0,1] op_sel_hi:[1,1] neg_lo:[0,1] neg_hi:[0,1]
	v_pk_add_f32 v[226:227], v[42:43], v[138:139] op_sel:[0,1] op_sel_hi:[1,1] neg_lo:[0,1] neg_hi:[0,1]
	v_pk_add_f32 v[228:229], v[44:45], v[138:139] op_sel:[0,1] op_sel_hi:[1,1] neg_lo:[0,1] neg_hi:[0,1]
	v_pk_add_f32 v[230:231], v[46:47], v[138:139] op_sel:[0,1] op_sel_hi:[1,1] neg_lo:[0,1] neg_hi:[0,1]
	v_pk_add_f32 v[232:233], v[48:49], v[138:139] op_sel:[0,1] op_sel_hi:[1,1] neg_lo:[0,1] neg_hi:[0,1]
	v_pk_add_f32 v[234:235], v[50:51], v[138:139] op_sel:[0,1] op_sel_hi:[1,1] neg_lo:[0,1] neg_hi:[0,1]
	v_exp_f32_e32 v200, v220
	v_exp_f32_e32 v201, v221
	v_exp_f32_e32 v202, v222
	v_exp_f32_e32 v203, v223
	v_exp_f32_e32 v204, v224
	v_exp_f32_e32 v205, v225
	v_exp_f32_e32 v206, v226
	v_exp_f32_e32 v207, v227
	v_add_u32_e32 v182, 0, v135
	v_exp_f32_e32 v208, v228
	ds_read_b64_tr_b16 v[40:41], v182 offset:55296
	ds_read_b64_tr_b16 v[42:43], v182 offset:55808
	v_exp_f32_e32 v209, v229
	v_add_u32_e32 v245, 0x6000, v182
	v_exp_f32_e32 v210, v230
	ds_read_b64_tr_b16 v[44:45], v245 offset:55296
	ds_read_b64_tr_b16 v[46:47], v245 offset:55808
	ds_read_b64_tr_b16 v[166:167], v182 offset:56320
	ds_read_b64_tr_b16 v[168:169], v182 offset:56832
	v_exp_f32_e32 v211, v231
	v_exp_f32_e32 v212, v232
	v_cvt_pk_bf16_f32 v36, v200, v201
	v_cvt_pk_bf16_f32 v37, v202, v203
	v_cvt_pk_bf16_f32 v38, v204, v205
	v_cvt_pk_bf16_f32 v39, v206, v207
	s_waitcnt lgkmcnt(4)
	v_mfma_f32_32x32x16_bf16 v[20:35], v[40:43], v[36:39], v[20:35]
	v_exp_f32_e32 v213, v233
	ds_read_b64_tr_b16 v[40:41], v245 offset:56320
	ds_read_b64_tr_b16 v[42:43], v245 offset:56832
	s_waitcnt lgkmcnt(4)
	v_mfma_f32_32x32x16_bf16 v[4:19], v[44:47], v[36:39], v[4:19]
	v_exp_f32_e32 v214, v234
	v_exp_f32_e32 v215, v235
	v_cvt_pk_bf16_f32 v36, v208, v209
	v_cvt_pk_bf16_f32 v37, v210, v211
	v_cvt_pk_bf16_f32 v38, v212, v213
	v_cvt_pk_bf16_f32 v39, v214, v215
	s_waitcnt lgkmcnt(2)
	v_mfma_f32_32x32x16_bf16 v[20:35], v[166:169], v[36:39], v[20:35]
	s_add_i32 s6, s6, 1
	s_waitcnt lgkmcnt(0)
	v_mfma_f32_32x32x16_bf16 v[4:19], v[40:43], v[36:39], v[4:19]
	v_pk_add_f32 v[236:237], v[200:201], v[202:203]
	v_pk_add_f32 v[238:239], v[204:205], v[206:207]
	v_pk_add_f32 v[240:241], v[208:209], v[210:211]
	v_pk_add_f32 v[242:243], v[212:213], v[214:215]
	v_pk_add_f32 v[236:237], v[236:237], v[238:239]
	v_pk_add_f32 v[240:241], v[240:241], v[242:243]
	v_pk_add_f32 v[236:237], v[236:237], v[240:241]
	v_add_f32_e32 v236, v236, v237
	v_add_f32_e32 v3, v3, v236
	v_add_u32_e32 v135, 0x800, v135
	v_add_u32_e32 v137, 0x1200, v137
	s_cmp_lt_u32 s6, 4
	v_add_u32_e32 v138, 0x80, v138
	s_cbranch_scc0 .LBB0_382
.LBB0_380:
	v_add_u32_e32 v244, 0x19800, v138
	ds_read2_b32 v[36:37], v244 offset1:1
	ds_read2_b32 v[38:39], v244 offset0:2 offset1:3
	ds_read2_b32 v[40:41], v244 offset0:8 offset1:9
	ds_read2_b32 v[42:43], v244 offset0:10 offset1:11
	v_add_u32_e32 v174, 0, v137
	ds_read_b128 v[166:169], v174
	ds_read2_b32 v[44:45], v244 offset0:16 offset1:17
	ds_read2_b32 v[46:47], v244 offset0:18 offset1:19
	ds_read2_b32 v[48:49], v244 offset0:24 offset1:25
	ds_read2_b32 v[50:51], v244 offset0:26 offset1:27
	ds_read_b128 v[170:173], v174 offset:32
	s_waitcnt lgkmcnt(1)
	v_mfma_f32_32x32x16_bf16 v[36:51], v[166:169], v[60:63], v[36:51]
	s_waitcnt lgkmcnt(0)
	v_mfma_f32_32x32x16_bf16 v[36:51], v[170:173], v[74:77], v[36:51]
	ds_read_b128 v[166:169], v174 offset:64
	ds_read_b128 v[170:173], v174 offset:96
	s_waitcnt lgkmcnt(1)
	v_mfma_f32_32x32x16_bf16 v[36:51], v[166:169], v[78:81], v[36:51]
	s_waitcnt lgkmcnt(0)
	v_mfma_f32_32x32x16_bf16 v[36:51], v[170:173], v[82:85], v[36:51]
	s_nop 11
	v_max3_f32 v166, v36, v37, v38
	v_max3_f32 v167, v39, v40, v41
	v_max3_f32 v168, v42, v43, v44
	v_max3_f32 v169, v45, v46, v47
	v_max3_f32 v170, v48, v49, v50
	v_max3_f32 v166, v166, v167, v51
	v_max3_f32 v168, v168, v169, v170
	v_max_f32_e32 v166, v166, v168
	v_mov_b32_e32 v167, v166
	s_nop 1
	v_permlane32_swap_b32_e32 v166, v167
	v_max_f32_e32 v166, v166, v167
	v_add_f32_e32 v167, 0x41000000, v139
	v_cmp_gt_f32_e32 vcc, v166, v167
	s_cbranch_vccz .LBB0_379
	v_max_f32_e32 v166, v166, v166
	v_max_f32_e32 v167, v139, v139
	v_max_f32_e32 v167, v167, v166
	v_sub_f32_e32 v139, v139, v167
	v_exp_f32_e32 v166, v139
	v_mov_b32_e32 v139, v167
	v_pk_mul_f32 v[34:35], v[34:35], v[166:167] op_sel_hi:[1,0]
	v_pk_mul_f32 v[32:33], v[32:33], v[166:167] op_sel_hi:[1,0]
	v_pk_mul_f32 v[30:31], v[30:31], v[166:167] op_sel_hi:[1,0]
	v_pk_mul_f32 v[28:29], v[28:29], v[166:167] op_sel_hi:[1,0]
	v_pk_mul_f32 v[26:27], v[26:27], v[166:167] op_sel_hi:[1,0]
	v_pk_mul_f32 v[24:25], v[24:25], v[166:167] op_sel_hi:[1,0]
	v_pk_mul_f32 v[22:23], v[22:23], v[166:167] op_sel_hi:[1,0]
	v_pk_mul_f32 v[20:21], v[20:21], v[166:167] op_sel_hi:[1,0]
	v_pk_mul_f32 v[18:19], v[18:19], v[166:167] op_sel_hi:[1,0]
	v_pk_mul_f32 v[16:17], v[16:17], v[166:167] op_sel_hi:[1,0]
	v_pk_mul_f32 v[14:15], v[14:15], v[166:167] op_sel_hi:[1,0]
	v_pk_mul_f32 v[12:13], v[12:13], v[166:167] op_sel_hi:[1,0]
	v_pk_mul_f32 v[10:11], v[10:11], v[166:167] op_sel_hi:[1,0]
	v_pk_mul_f32 v[8:9], v[8:9], v[166:167] op_sel_hi:[1,0]
	v_pk_mul_f32 v[6:7], v[6:7], v[166:167] op_sel_hi:[1,0]
	v_pk_mul_f32 v[4:5], v[4:5], v[166:167] op_sel_hi:[1,0]
	v_mul_f32_e32 v3, v3, v166
	s_branch .LBB0_379

; #define LAS __attribute__((address_space(3)))
; template <bool BAND, int OUTMODE>
; __device__ __forceinline__ void compute(LAS unsigned char* lds, const bf16x8 (&qr)[4], int tid, int mq0, int dil, int res, int kt_min, int bias_tab, float sink2,
;                                         bf16* ob, int opitch, float* lsep) {
;     ...
;             for (int i = 0; i < 16; ++i) S[i] = bl[32 * t + (i & 3) + 8 * (i >> 2)];
;         } else {
; #pragma unroll
;             for (int i = 0; i < 16; ++i) S[i] = 0.f;
;         }
; #pragma unroll
;         for (int s = 0; s < 4; ++s) { const bf16x8 kf = *(const LAS bf16x8*)(kb + t * 32 * KSTR + s * 32); S = __builtin_amdgcn_mfma_f32_32x32x16_bf16(kf, qr[s], S, 0, 0, 0); }
;         float m0 = fmaxf(fmaxf(S[0], S[1]), fmaxf(S[2], S[3])), m1 = fmaxf(fmaxf(S[4], S[5]), fmaxf(S[6], S[7])), m2 = fmaxf(fmaxf(S[8], S[9]), fmaxf(S[10], S[11])), m3 = fmaxf(fmaxf(S[12], S[13]), fmaxf(S[14], S[15]));
;         const float mt = xhalf_max(fmaxf(fmaxf(m0, m1), fmaxf(m2, m3)));
;         if (__any(mt > mref + THR)) {
;             const float mnew = fmaxf(mref, mt), f = __builtin_amdgcn_exp2f(mref - mnew);
;             mref = mnew; l *= f;
; #pragma unroll
;             for (int i = 0; i < 16; ++i) { o0[i] *= f; o1[i] *= f; }
;         }
; #pragma unroll
;         for (int i = 0; i < 16; ++i) { const float p = __builtin_amdgcn_exp2f(S[i] - mref); S[i] = p; l += p; }
; #pragma unroll
;         for (int s = 0; s < 2; ++s) {
;             v4u pw; pw.x = cvtpk(S[8 * s + 0], S[8 * s + 1]); pw.y = cvtpk(S[8 * s + 2], S[8 * s + 3]); pw.z = cvtpk(S[8 * s + 4], S[8 * s + 5]); pw.w = cvtpk(S[8 * s + 6], S[8 * s + 7]);
;             const bf16x8 pa = __builtin_bit_cast(bf16x8, pw);
;             const LAS unsigned char* vp = vb + (32 * t + 16 * s) * 64;
;             const s16x4 a0 = vtr(vp), a1 = vtr(vp + 8 * 64), b0 = vtr(vp + VPLANE), b1 = vtr(vp + VPLANE + 8 * 64);
;             const bf16x8 v0 = __builtin_shufflevector(a0, a1, 0, 1, 2, 3, 4, 5, 6, 7), v1 = __builtin_shufflevector(b0, b1, 0, 1, 2, 3, 4, 5, 6, 7);
;             o0 = __builtin_amdgcn_mfma_f32_32x32x16_bf16(v0, pa, o0, 0, 0, 0);
;             o1 = __builtin_amdgcn_mfma_f32_32x32x16_bf16(v1, pa, o1, 0, 0, 0);
;         }
;     }
.LBB0_387:
	v_pk_add_f32 v[220:221], v[50:51], v[134:135] op_sel:[0,1] op_sel_hi:[1,1] neg_lo:[0,1] neg_hi:[0,1]
	v_pk_add_f32 v[222:223], v[52:53], v[134:135] op_sel:[0,1] op_sel_hi:[1,1] neg_lo:[0,1] neg_hi:[0,1]
	v_pk_add_f32 v[224:225], v[54:55], v[134:135] op_sel:[0,1] op_sel_hi:[1,1] neg_lo:[0,1] neg_hi:[0,1]
	v_pk_add_f32 v[226:227], v[56:57], v[134:135] op_sel:[0,1] op_sel_hi:[1,1] neg_lo:[0,1] neg_hi:[0,1]
	v_pk_add_f32 v[228:229], v[58:59], v[134:135] op_sel:[0,1] op_sel_hi:[1,1] neg_lo:[0,1] neg_hi:[0,1]
	v_pk_add_f32 v[230:231], v[60:61], v[134:135] op_sel:[0,1] op_sel_hi:[1,1] neg_lo:[0,1] neg_hi:[0,1]
	v_pk_add_f32 v[232:233], v[62:63], v[134:135] op_sel:[0,1] op_sel_hi:[1,1] neg_lo:[0,1] neg_hi:[0,1]
	v_pk_add_f32 v[234:235], v[64:65], v[134:135] op_sel:[0,1] op_sel_hi:[1,1] neg_lo:[0,1] neg_hi:[0,1]
	v_exp_f32_e32 v201, v221
	v_exp_f32_e32 v202, v222
	v_exp_f32_e32 v203, v223
	v_exp_f32_e32 v204, v224
	v_exp_f32_e32 v205, v225
	v_exp_f32_e32 v206, v226
	v_exp_f32_e32 v207, v227
	v_add_u32_e32 v137, 0, v131
	v_exp_f32_e32 v200, v220
	v_exp_f32_e32 v208, v228
	ds_read_b64_tr_b16 v[8:9], v137 offset:55296
	ds_read_b64_tr_b16 v[10:11], v137 offset:55808
	v_exp_f32_e32 v209, v229
	v_add_u32_e32 v245, 0x6000, v137
	v_exp_f32_e32 v210, v230
	ds_read_b64_tr_b16 v[12:13], v245 offset:55296
	ds_read_b64_tr_b16 v[14:15], v245 offset:55808
	ds_read_b64_tr_b16 v[50:51], v137 offset:56320
	ds_read_b64_tr_b16 v[52:53], v137 offset:56832
	v_exp_f32_e32 v211, v231
	v_exp_f32_e32 v212, v232
	v_cvt_pk_bf16_f32 v4, v200, v201
	v_cvt_pk_bf16_f32 v5, v202, v203
	v_cvt_pk_bf16_f32 v6, v204, v205
	v_cvt_pk_bf16_f32 v7, v206, v207
	s_waitcnt lgkmcnt(4)
	v_mfma_f32_32x32x16_bf16 v[34:49], v[8:11], v[4:7], v[34:49]
	v_exp_f32_e32 v213, v233
	ds_read_b64_tr_b16 v[8:9], v245 offset:56320
	ds_read_b64_tr_b16 v[10:11], v245 offset:56832
	s_waitcnt lgkmcnt(4)
	v_mfma_f32_32x32x16_bf16 v[18:33], v[12:15], v[4:7], v[18:33]
	v_exp_f32_e32 v214, v234
	v_exp_f32_e32 v215, v235
	v_cvt_pk_bf16_f32 v4, v208, v209
	v_cvt_pk_bf16_f32 v5, v210, v211
	v_cvt_pk_bf16_f32 v6, v212, v213
	v_cvt_pk_bf16_f32 v7, v214, v215
	s_waitcnt lgkmcnt(2)
	v_mfma_f32_32x32x16_bf16 v[34:49], v[50:53], v[4:7], v[34:49]
	s_add_i32 s5, s5, 1
	s_waitcnt lgkmcnt(0)
	v_mfma_f32_32x32x16_bf16 v[18:33], v[8:11], v[4:7], v[18:33]
	v_pk_add_f32 v[236:237], v[200:201], v[202:203]
	v_pk_add_f32 v[238:239], v[204:205], v[206:207]
	v_pk_add_f32 v[240:241], v[208:209], v[210:211]
	v_pk_add_f32 v[242:243], v[212:213], v[214:215]
	v_pk_add_f32 v[236:237], v[236:237], v[238:239]
	v_pk_add_f32 v[240:241], v[240:241], v[242:243]
	v_pk_add_f32 v[236:237], v[236:237], v[240:241]
	v_add_f32_e32 v236, v236, v237
	v_add_f32_e32 v3, v3, v236
	v_add_u32_e32 v131, 0x800, v131
	v_add_u32_e32 v132, 0x1200, v132
	s_cmp_lt_u32 s5, 4
	v_add_u32_e32 v133, 0x80, v133
	s_cbranch_scc0 .LBB0_390
.LBB0_388:
	v_add_u32_e32 v244, 0x19800, v133
	ds_read2_b32 v[50:51], v244 offset1:1
	ds_read2_b32 v[52:53], v244 offset0:2 offset1:3
	ds_read2_b32 v[54:55], v244 offset0:8 offset1:9
	ds_read2_b32 v[56:57], v244 offset0:10 offset1:11
	v_add_u32_e32 v12, 0, v132
	ds_read_b128 v[4:7], v12
	ds_read2_b32 v[58:59], v244 offset0:16 offset1:17
	ds_read2_b32 v[60:61], v244 offset0:18 offset1:19
	ds_read2_b32 v[62:63], v244 offset0:24 offset1:25
	ds_read2_b32 v[64:65], v244 offset0:26 offset1:27
	ds_read_b128 v[8:11], v12 offset:32
	s_waitcnt lgkmcnt(1)
	v_mfma_f32_32x32x16_bf16 v[50:65], v[4:7], v[86:89], v[50:65]
	s_waitcnt lgkmcnt(0)
	v_mfma_f32_32x32x16_bf16 v[50:65], v[8:11], v[90:93], v[50:65]
	ds_read_b128 v[4:7], v12 offset:64
	ds_read_b128 v[8:11], v12 offset:96
	s_waitcnt lgkmcnt(1)
	v_mfma_f32_32x32x16_bf16 v[50:65], v[4:7], v[94:97], v[50:65]
	s_waitcnt lgkmcnt(0)
	v_mfma_f32_32x32x16_bf16 v[50:65], v[8:11], v[98:101], v[50:65]
	s_nop 11
	v_max3_f32 v2, v50, v51, v52
	v_max3_f32 v4, v53, v54, v55
	v_max3_f32 v5, v56, v57, v58
	v_max3_f32 v6, v59, v60, v61
	v_max3_f32 v7, v62, v63, v64
	v_max3_f32 v2, v2, v4, v65
	v_max3_f32 v5, v5, v6, v7
	v_max_f32_e32 v2, v2, v5
	v_mov_b32_e32 v4, v2
	s_nop 1
	v_permlane32_swap_b32_e32 v2, v4
	v_max_f32_e32 v2, v2, v4
	v_add_f32_e32 v4, 0x41000000, v135
	v_cmp_gt_f32_e32 vcc, v2, v4
	s_cbranch_vccz .LBB0_387
	v_max_f32_e32 v2, v2, v2
	v_max_f32_e32 v4, v135, v135
	v_max_f32_e32 v4, v4, v2
	v_sub_f32_e32 v2, v135, v4
	v_exp_f32_e32 v2, v2
	v_mov_b32_e32 v135, v4
	v_pk_mul_f32 v[48:49], v[48:49], v[2:3] op_sel_hi:[1,0]
	v_pk_mul_f32 v[46:47], v[46:47], v[2:3] op_sel_hi:[1,0]
	v_pk_mul_f32 v[44:45], v[44:45], v[2:3] op_sel_hi:[1,0]
	v_pk_mul_f32 v[42:43], v[42:43], v[2:3] op_sel_hi:[1,0]
	v_pk_mul_f32 v[40:41], v[40:41], v[2:3] op_sel_hi:[1,0]
	v_pk_mul_f32 v[38:39], v[38:39], v[2:3] op_sel_hi:[1,0]
	v_pk_mul_f32 v[36:37], v[36:37], v[2:3] op_sel_hi:[1,0]
	v_pk_mul_f32 v[34:35], v[34:35], v[2:3] op_sel_hi:[1,0]
	v_pk_mul_f32 v[32:33], v[32:33], v[2:3] op_sel_hi:[1,0]
	v_pk_mul_f32 v[30:31], v[30:31], v[2:3] op_sel_hi:[1,0]
	v_pk_mul_f32 v[28:29], v[28:29], v[2:3] op_sel_hi:[1,0]
	v_pk_mul_f32 v[26:27], v[26:27], v[2:3] op_sel_hi:[1,0]
	v_pk_mul_f32 v[24:25], v[24:25], v[2:3] op_sel_hi:[1,0]
	v_pk_mul_f32 v[22:23], v[22:23], v[2:3] op_sel_hi:[1,0]
	v_pk_mul_f32 v[20:21], v[20:21], v[2:3] op_sel_hi:[1,0]
	v_pk_mul_f32 v[18:19], v[18:19], v[2:3] op_sel_hi:[1,0]
	v_mul_f32_e32 v3, v3, v2
	s_branch .LBB0_387

; #define LAS __attribute__((address_space(3)))
; __device__ __forceinline__ unsigned cvtpk(float lo, float hi) { f32x2_t v = {lo, hi}; bf16x2_t b = __builtin_convertvector(v, bf16x2_t); return __builtin_bit_cast(unsigned, b); }
; __device__ __forceinline__ s16x4 vtr(const LAS unsigned char* p) { return __builtin_bit_cast(s16x4, __builtin_amdgcn_ds_read_tr16_b64_v4i16((LAS v4i16_t*)p)); }
; template <bool BAND, int OUTMODE>
; __device__ __forceinline__ void compute(LAS unsigned char* lds, const bf16x8 (&qr)[4], int tid, int mq0, int dil, int res, int kt_min, int bias_tab, float sink2,
;                                         bf16* ob, int opitch, float* lsep) {
;     ...
;             for (int i = 0; i < 16; ++i) { o0[i] *= f; o1[i] *= f; }
;         }
; #pragma unroll
;         for (int i = 0; i < 16; ++i) { const float p = __builtin_amdgcn_exp2f(S[i] - mref); S[i] = p; l += p; }
; #pragma unroll
;         for (int s = 0; s < 2; ++s) {
;             v4u pw; pw.x = cvtpk(S[8 * s + 0], S[8 * s + 1]); pw.y = cvtpk(S[8 * s + 2], S[8 * s + 3]); pw.z = cvtpk(S[8 * s + 4], S[8 * s + 5]); pw.w = cvtpk(S[8 * s + 6], S[8 * s + 7]);
;             const bf16x8 pa = __builtin_bit_cast(bf16x8, pw);
;             const LAS unsigned char* vp = vb + (32 * t + 16 * s) * 64;
;             const s16x4 a0 = vtr(vp), a1 = vtr(vp + 8 * 64), b0 = vtr(vp + VPLANE), b1 = vtr(vp + VPLANE + 8 * 64);
;             const bf16x8 v0 = __builtin_shufflevector(a0, a1, 0, 1, 2, 3, 4, 5, 6, 7), v1 = __builtin_shufflevector(b0, b1, 0, 1, 2, 3, 4, 5, 6, 7);
;             o0 = __builtin_amdgcn_mfma_f32_32x32x16_bf16(v0, pa, o0, 0, 0, 0);
;             o1 = __builtin_amdgcn_mfma_f32_32x32x16_bf16(v1, pa, o1, 0, 0, 0);
;         }
;     }
.LBB0_393:
	v_pk_add_f32 v[220:221], v[34:35], v[52:53] op_sel_hi:[1,0] neg_lo:[0,1] neg_hi:[0,1]
	v_pk_add_f32 v[222:223], v[36:37], v[52:53] op_sel_hi:[1,0] neg_lo:[0,1] neg_hi:[0,1]
	v_pk_add_f32 v[224:225], v[38:39], v[52:53] op_sel_hi:[1,0] neg_lo:[0,1] neg_hi:[0,1]
	v_pk_add_f32 v[226:227], v[40:41], v[52:53] op_sel_hi:[1,0] neg_lo:[0,1] neg_hi:[0,1]
	v_pk_add_f32 v[228:229], v[42:43], v[52:53] op_sel_hi:[1,0] neg_lo:[0,1] neg_hi:[0,1]
	v_pk_add_f32 v[230:231], v[44:45], v[52:53] op_sel_hi:[1,0] neg_lo:[0,1] neg_hi:[0,1]
	v_pk_add_f32 v[232:233], v[46:47], v[52:53] op_sel_hi:[1,0] neg_lo:[0,1] neg_hi:[0,1]
	v_pk_add_f32 v[234:235], v[48:49], v[52:53] op_sel_hi:[1,0] neg_lo:[0,1] neg_hi:[0,1]
	v_exp_f32_e32 v200, v220
	v_exp_f32_e32 v201, v221
	v_exp_f32_e32 v202, v222
	v_exp_f32_e32 v203, v223
	v_exp_f32_e32 v204, v224
	v_exp_f32_e32 v205, v225
	v_exp_f32_e32 v206, v226
	v_exp_f32_e32 v207, v227
	v_add_u32_e32 v69, v51, v134
	v_exp_f32_e32 v208, v228
	ds_read_b64_tr_b16 v[38:39], v69 offset:55296
	ds_read_b64_tr_b16 v[40:41], v69 offset:55808
	v_exp_f32_e32 v209, v229
	v_add_u32_e32 v245, 0x6000, v69
	v_exp_f32_e32 v210, v230
	ds_read_b64_tr_b16 v[42:43], v245 offset:55296
	ds_read_b64_tr_b16 v[44:45], v245 offset:55808
	ds_read_b64_tr_b16 v[54:55], v69 offset:56320
	ds_read_b64_tr_b16 v[56:57], v69 offset:56832
	v_exp_f32_e32 v211, v231
	v_exp_f32_e32 v212, v232
	v_cvt_pk_bf16_f32 v34, v200, v201
	v_cvt_pk_bf16_f32 v35, v202, v203
	v_cvt_pk_bf16_f32 v36, v204, v205
	v_cvt_pk_bf16_f32 v37, v206, v207
	s_add_i32 s4, s4, -1
	s_waitcnt lgkmcnt(4)
	v_mfma_f32_32x32x16_bf16 v[18:33], v[38:41], v[34:37], v[18:33]
	v_exp_f32_e32 v213, v233
	ds_read_b64_tr_b16 v[38:39], v245 offset:56320
	ds_read_b64_tr_b16 v[40:41], v245 offset:56832
	v_add_u32_e32 v51, 0x800, v51
	s_cmp_lg_u32 s4, 0
	s_waitcnt lgkmcnt(4)
	v_mfma_f32_32x32x16_bf16 v[2:17], v[42:45], v[34:37], v[2:17]
	v_exp_f32_e32 v214, v234
	v_exp_f32_e32 v215, v235
	v_cvt_pk_bf16_f32 v34, v208, v209
	v_cvt_pk_bf16_f32 v35, v210, v211
	v_cvt_pk_bf16_f32 v36, v212, v213
	v_cvt_pk_bf16_f32 v37, v214, v215
	v_add_u32_e32 v50, 0x1200, v50
	s_waitcnt lgkmcnt(2)
	v_mfma_f32_32x32x16_bf16 v[18:33], v[54:57], v[34:37], v[18:33]
	s_waitcnt lgkmcnt(0)
	v_mfma_f32_32x32x16_bf16 v[2:17], v[38:41], v[34:37], v[2:17]
	v_pk_add_f32 v[236:237], v[200:201], v[202:203]
	v_pk_add_f32 v[238:239], v[204:205], v[206:207]
	v_pk_add_f32 v[240:241], v[208:209], v[210:211]
	v_pk_add_f32 v[242:243], v[212:213], v[214:215]
	v_pk_add_f32 v[236:237], v[236:237], v[238:239]
	v_pk_add_f32 v[240:241], v[240:241], v[242:243]
	v_pk_add_f32 v[236:237], v[236:237], v[240:241]
	v_add_f32_e32 v236, v236, v237
	v_add_f32_e32 v139, v139, v236
	s_cbranch_scc0 .LBB0_396

; #define LAS __attribute__((address_space(3)))
; template <bool BAND, int OUTMODE>
; __device__ __forceinline__ void compute(LAS unsigned char* lds, const bf16x8 (&qr)[4], int tid, int mq0, int dil, int res, int kt_min, int bias_tab, float sink2,
;                                         bf16* ob, int opitch, float* lsep) {
;     ...
;             for (int i = 0; i < 16; ++i) S[i] = bl[32 * t + (i & 3) + 8 * (i >> 2)];
;         } else {
; #pragma unroll
;             for (int i = 0; i < 16; ++i) S[i] = 0.f;
;         }
; #pragma unroll
;         for (int s = 0; s < 4; ++s) { const bf16x8 kf = *(const LAS bf16x8*)(kb + t * 32 * KSTR + s * 32); S = __builtin_amdgcn_mfma_f32_32x32x16_bf16(kf, qr[s], S, 0, 0, 0); }
;         float m0 = fmaxf(fmaxf(S[0], S[1]), fmaxf(S[2], S[3])), m1 = fmaxf(fmaxf(S[4], S[5]), fmaxf(S[6], S[7])), m2 = fmaxf(fmaxf(S[8], S[9]), fmaxf(S[10], S[11])), m3 = fmaxf(fmaxf(S[12], S[13]), fmaxf(S[14], S[15]));
;         const float mt = xhalf_max(fmaxf(fmaxf(m0, m1), fmaxf(m2, m3)));
;         if (__any(mt > mref + THR)) {
;             const float mnew = fmaxf(mref, mt), f = __builtin_amdgcn_exp2f(mref - mnew);
;             mref = mnew; l *= f;
; #pragma unroll
;             for (int i = 0; i < 16; ++i) { o0[i] *= f; o1[i] *= f; }
;         }
; #pragma unroll
;         for (int i = 0; i < 16; ++i) { const float p = __builtin_amdgcn_exp2f(S[i] - mref); S[i] = p; l += p; }
; #pragma unroll
;         for (int s = 0; s < 2; ++s) {
;             v4u pw; pw.x = cvtpk(S[8 * s + 0], S[8 * s + 1]); pw.y = cvtpk(S[8 * s + 2], S[8 * s + 3]); pw.z = cvtpk(S[8 * s + 4], S[8 * s + 5]); pw.w = cvtpk(S[8 * s + 6], S[8 * s + 7]);
;             const bf16x8 pa = __builtin_bit_cast(bf16x8, pw);
;             const LAS unsigned char* vp = vb + (32 * t + 16 * s) * 64;
;             const s16x4 a0 = vtr(vp), a1 = vtr(vp + 8 * 64), b0 = vtr(vp + VPLANE), b1 = vtr(vp + VPLANE + 8 * 64);
;             const bf16x8 v0 = __builtin_shufflevector(a0, a1, 0, 1, 2, 3, 4, 5, 6, 7), v1 = __builtin_shufflevector(b0, b1, 0, 1, 2, 3, 4, 5, 6, 7);
;             o0 = __builtin_amdgcn_mfma_f32_32x32x16_bf16(v0, pa, o0, 0, 0, 0);
;             o1 = __builtin_amdgcn_mfma_f32_32x32x16_bf16(v1, pa, o1, 0, 0, 0);
;         }
;     }
.LBB0_940:
	v_pk_add_f32 v[220:221], v[36:37], v[164:165] op_sel:[0,1] op_sel_hi:[1,1] neg_lo:[0,1] neg_hi:[0,1]
	v_pk_add_f32 v[222:223], v[38:39], v[164:165] op_sel:[0,1] op_sel_hi:[1,1] neg_lo:[0,1] neg_hi:[0,1]
	v_pk_add_f32 v[224:225], v[40:41], v[164:165] op_sel:[0,1] op_sel_hi:[1,1] neg_lo:[0,1] neg_hi:[0,1]
	v_pk_add_f32 v[226:227], v[42:43], v[164:165] op_sel:[0,1] op_sel_hi:[1,1] neg_lo:[0,1] neg_hi:[0,1]
	v_pk_add_f32 v[228:229], v[44:45], v[164:165] op_sel:[0,1] op_sel_hi:[1,1] neg_lo:[0,1] neg_hi:[0,1]
	v_pk_add_f32 v[230:231], v[46:47], v[164:165] op_sel:[0,1] op_sel_hi:[1,1] neg_lo:[0,1] neg_hi:[0,1]
	v_pk_add_f32 v[232:233], v[48:49], v[164:165] op_sel:[0,1] op_sel_hi:[1,1] neg_lo:[0,1] neg_hi:[0,1]
	v_pk_add_f32 v[234:235], v[50:51], v[164:165] op_sel:[0,1] op_sel_hi:[1,1] neg_lo:[0,1] neg_hi:[0,1]
	v_exp_f32_e32 v200, v220
	v_exp_f32_e32 v201, v221
	v_exp_f32_e32 v202, v222
	v_exp_f32_e32 v203, v223
	v_exp_f32_e32 v204, v224
	v_exp_f32_e32 v205, v225
	v_exp_f32_e32 v206, v226
	v_exp_f32_e32 v207, v227
	v_add_u32_e32 v184, 0, v135
	v_exp_f32_e32 v208, v228
	ds_read_b64_tr_b16 v[40:41], v184 offset:55296
	ds_read_b64_tr_b16 v[42:43], v184 offset:55808
	v_exp_f32_e32 v209, v229
	v_add_u32_e32 v245, 0x6000, v184
	v_exp_f32_e32 v210, v230
	ds_read_b64_tr_b16 v[44:45], v245 offset:55296
	ds_read_b64_tr_b16 v[46:47], v245 offset:55808
	ds_read_b64_tr_b16 v[168:169], v184 offset:56320
	ds_read_b64_tr_b16 v[170:171], v184 offset:56832
	v_exp_f32_e32 v211, v231
	v_exp_f32_e32 v212, v232
	v_cvt_pk_bf16_f32 v36, v200, v201
	v_cvt_pk_bf16_f32 v37, v202, v203
	v_cvt_pk_bf16_f32 v38, v204, v205
	v_cvt_pk_bf16_f32 v39, v206, v207
	s_waitcnt lgkmcnt(4)
	v_mfma_f32_32x32x16_bf16 v[20:35], v[40:43], v[36:39], v[20:35]
	v_exp_f32_e32 v213, v233
	ds_read_b64_tr_b16 v[40:41], v245 offset:56320
	ds_read_b64_tr_b16 v[42:43], v245 offset:56832
	s_waitcnt lgkmcnt(4)
	v_mfma_f32_32x32x16_bf16 v[4:19], v[44:47], v[36:39], v[4:19]
	v_exp_f32_e32 v214, v234
	v_exp_f32_e32 v215, v235
	v_cvt_pk_bf16_f32 v36, v208, v209
	v_cvt_pk_bf16_f32 v37, v210, v211
	v_cvt_pk_bf16_f32 v38, v212, v213
	v_cvt_pk_bf16_f32 v39, v214, v215
	s_waitcnt lgkmcnt(2)
	v_mfma_f32_32x32x16_bf16 v[20:35], v[168:171], v[36:39], v[20:35]
	s_add_i32 s6, s6, 1
	s_waitcnt lgkmcnt(0)
	v_mfma_f32_32x32x16_bf16 v[4:19], v[40:43], v[36:39], v[4:19]
	v_pk_add_f32 v[236:237], v[200:201], v[202:203]
	v_pk_add_f32 v[238:239], v[204:205], v[206:207]
	v_pk_add_f32 v[240:241], v[208:209], v[210:211]
	v_pk_add_f32 v[242:243], v[212:213], v[214:215]
	v_pk_add_f32 v[236:237], v[236:237], v[238:239]
	v_pk_add_f32 v[240:241], v[240:241], v[242:243]
	v_pk_add_f32 v[236:237], v[236:237], v[240:241]
	v_add_f32_e32 v236, v236, v237
	v_add_f32_e32 v3, v3, v236
	v_add_u32_e32 v135, 0x800, v135
	v_add_u32_e32 v149, 0x1200, v149
	s_cmp_gt_u32 s6, 3
	v_add_u32_e32 v167, 0x80, v167
	s_cbranch_scc1 .LBB0_943
.LBB0_941:
	v_add_u32_e32 v244, 0x19800, v167
	ds_read2_b32 v[36:37], v244 offset1:1
	ds_read2_b32 v[38:39], v244 offset0:2 offset1:3
	ds_read2_b32 v[40:41], v244 offset0:8 offset1:9
	ds_read2_b32 v[42:43], v244 offset0:10 offset1:11
	v_add_u32_e32 v176, 0, v149
	ds_read_b128 v[168:171], v176
	ds_read2_b32 v[44:45], v244 offset0:16 offset1:17
	ds_read2_b32 v[46:47], v244 offset0:18 offset1:19
	ds_read2_b32 v[48:49], v244 offset0:24 offset1:25
	ds_read2_b32 v[50:51], v244 offset0:26 offset1:27
	ds_read_b128 v[172:175], v176 offset:32
	s_waitcnt vmcnt(17) lgkmcnt(1)
	v_mfma_f32_32x32x16_bf16 v[36:51], v[168:171], v[118:121], v[36:51]
	s_waitcnt vmcnt(16) lgkmcnt(0)
	v_mfma_f32_32x32x16_bf16 v[36:51], v[172:175], v[122:125], v[36:51]
	ds_read_b128 v[168:171], v176 offset:64
	ds_read_b128 v[172:175], v176 offset:96
	s_waitcnt vmcnt(15) lgkmcnt(1)
	v_mfma_f32_32x32x16_bf16 v[36:51], v[168:171], v[126:129], v[36:51]
	s_waitcnt vmcnt(14) lgkmcnt(0)
	v_mfma_f32_32x32x16_bf16 v[36:51], v[172:175], v[130:133], v[36:51]
	s_nop 11
	v_max3_f32 v168, v36, v37, v38
	v_max3_f32 v169, v39, v40, v41
	v_max3_f32 v170, v42, v43, v44
	v_max3_f32 v171, v45, v46, v47
	v_max3_f32 v172, v48, v49, v50
	v_max3_f32 v168, v168, v169, v51
	v_max3_f32 v170, v170, v171, v172
	v_max_f32_e32 v168, v168, v170
	v_mov_b32_e32 v169, v168
	s_nop 1
	v_permlane32_swap_b32_e32 v168, v169
	v_max_f32_e32 v168, v168, v169
	v_add_f32_e32 v169, 0x41000000, v165
	v_cmp_gt_f32_e32 vcc, v168, v169
	s_cbranch_vccz .LBB0_940
	v_max_f32_e32 v168, v168, v168
	v_max_f32_e32 v169, v165, v165
	v_max_f32_e32 v169, v169, v168
	v_sub_f32_e32 v165, v165, v169
	v_exp_f32_e32 v168, v165
	v_mov_b32_e32 v165, v169
	v_pk_mul_f32 v[34:35], v[34:35], v[168:169] op_sel_hi:[1,0]
	v_pk_mul_f32 v[32:33], v[32:33], v[168:169] op_sel_hi:[1,0]
	v_pk_mul_f32 v[30:31], v[30:31], v[168:169] op_sel_hi:[1,0]
	v_pk_mul_f32 v[28:29], v[28:29], v[168:169] op_sel_hi:[1,0]
	v_pk_mul_f32 v[26:27], v[26:27], v[168:169] op_sel_hi:[1,0]
	v_pk_mul_f32 v[24:25], v[24:25], v[168:169] op_sel_hi:[1,0]
	v_pk_mul_f32 v[22:23], v[22:23], v[168:169] op_sel_hi:[1,0]
	v_pk_mul_f32 v[20:21], v[20:21], v[168:169] op_sel_hi:[1,0]
	v_pk_mul_f32 v[18:19], v[18:19], v[168:169] op_sel_hi:[1,0]
	v_pk_mul_f32 v[16:17], v[16:17], v[168:169] op_sel_hi:[1,0]
	v_pk_mul_f32 v[14:15], v[14:15], v[168:169] op_sel_hi:[1,0]
	v_pk_mul_f32 v[12:13], v[12:13], v[168:169] op_sel_hi:[1,0]
	v_pk_mul_f32 v[10:11], v[10:11], v[168:169] op_sel_hi:[1,0]
	v_pk_mul_f32 v[8:9], v[8:9], v[168:169] op_sel_hi:[1,0]
	v_pk_mul_f32 v[6:7], v[6:7], v[168:169] op_sel_hi:[1,0]
	v_pk_mul_f32 v[4:5], v[4:5], v[168:169] op_sel_hi:[1,0]
	v_mul_f32_e32 v3, v3, v168
	s_branch .LBB0_940

; #define LAS __attribute__((address_space(3)))
; template <bool BAND, int OUTMODE>
; __device__ __forceinline__ void compute(LAS unsigned char* lds, const bf16x8 (&qr)[4], int tid, int mq0, int dil, int res, int kt_min, int bias_tab, float sink2,
;                                         bf16* ob, int opitch, float* lsep) {
;     ...
;             for (int i = 0; i < 16; ++i) S[i] = bl[32 * t + (i & 3) + 8 * (i >> 2)];
;         } else {
; #pragma unroll
;             for (int i = 0; i < 16; ++i) S[i] = 0.f;
;         }
; #pragma unroll
;         for (int s = 0; s < 4; ++s) { const bf16x8 kf = *(const LAS bf16x8*)(kb + t * 32 * KSTR + s * 32); S = __builtin_amdgcn_mfma_f32_32x32x16_bf16(kf, qr[s], S, 0, 0, 0); }
;         float m0 = fmaxf(fmaxf(S[0], S[1]), fmaxf(S[2], S[3])), m1 = fmaxf(fmaxf(S[4], S[5]), fmaxf(S[6], S[7])), m2 = fmaxf(fmaxf(S[8], S[9]), fmaxf(S[10], S[11])), m3 = fmaxf(fmaxf(S[12], S[13]), fmaxf(S[14], S[15]));
;         const float mt = xhalf_max(fmaxf(fmaxf(m0, m1), fmaxf(m2, m3)));
;         if (__any(mt > mref + THR)) {
;             const float mnew = fmaxf(mref, mt), f = __builtin_amdgcn_exp2f(mref - mnew);
;             mref = mnew; l *= f;
; #pragma unroll
;             for (int i = 0; i < 16; ++i) { o0[i] *= f; o1[i] *= f; }
;         }
; #pragma unroll
;         for (int i = 0; i < 16; ++i) { const float p = __builtin_amdgcn_exp2f(S[i] - mref); S[i] = p; l += p; }
; #pragma unroll
;         for (int s = 0; s < 2; ++s) {
;             v4u pw; pw.x = cvtpk(S[8 * s + 0], S[8 * s + 1]); pw.y = cvtpk(S[8 * s + 2], S[8 * s + 3]); pw.z = cvtpk(S[8 * s + 4], S[8 * s + 5]); pw.w = cvtpk(S[8 * s + 6], S[8 * s + 7]);
;             const bf16x8 pa = __builtin_bit_cast(bf16x8, pw);
;             const LAS unsigned char* vp = vb + (32 * t + 16 * s) * 64;
;             const s16x4 a0 = vtr(vp), a1 = vtr(vp + 8 * 64), b0 = vtr(vp + VPLANE), b1 = vtr(vp + VPLANE + 8 * 64);
;             const bf16x8 v0 = __builtin_shufflevector(a0, a1, 0, 1, 2, 3, 4, 5, 6, 7), v1 = __builtin_shufflevector(b0, b1, 0, 1, 2, 3, 4, 5, 6, 7);
;             o0 = __builtin_amdgcn_mfma_f32_32x32x16_bf16(v0, pa, o0, 0, 0, 0);
;             o1 = __builtin_amdgcn_mfma_f32_32x32x16_bf16(v1, pa, o1, 0, 0, 0);
;         }
;     }
.LBB0_950:
	v_pk_add_f32 v[220:221], v[36:37], v[64:65] op_sel:[0,1] op_sel_hi:[1,1] neg_lo:[0,1] neg_hi:[0,1]
	v_pk_add_f32 v[222:223], v[38:39], v[64:65] op_sel:[0,1] op_sel_hi:[1,1] neg_lo:[0,1] neg_hi:[0,1]
	v_pk_add_f32 v[224:225], v[40:41], v[64:65] op_sel:[0,1] op_sel_hi:[1,1] neg_lo:[0,1] neg_hi:[0,1]
	v_pk_add_f32 v[226:227], v[42:43], v[64:65] op_sel:[0,1] op_sel_hi:[1,1] neg_lo:[0,1] neg_hi:[0,1]
	v_pk_add_f32 v[228:229], v[44:45], v[64:65] op_sel:[0,1] op_sel_hi:[1,1] neg_lo:[0,1] neg_hi:[0,1]
	v_pk_add_f32 v[230:231], v[46:47], v[64:65] op_sel:[0,1] op_sel_hi:[1,1] neg_lo:[0,1] neg_hi:[0,1]
	v_pk_add_f32 v[232:233], v[48:49], v[64:65] op_sel:[0,1] op_sel_hi:[1,1] neg_lo:[0,1] neg_hi:[0,1]
	v_pk_add_f32 v[234:235], v[50:51], v[64:65] op_sel:[0,1] op_sel_hi:[1,1] neg_lo:[0,1] neg_hi:[0,1]
	v_exp_f32_e32 v200, v220
	v_exp_f32_e32 v201, v221
	v_exp_f32_e32 v202, v222
	v_exp_f32_e32 v203, v223
	v_exp_f32_e32 v204, v224
	v_exp_f32_e32 v205, v225
	v_exp_f32_e32 v206, v226
	v_exp_f32_e32 v207, v227
	v_add_u32_e32 v182, 0, v137
	v_exp_f32_e32 v208, v228
	ds_read_b64_tr_b16 v[40:41], v182 offset:55296
	ds_read_b64_tr_b16 v[42:43], v182 offset:55808
	v_exp_f32_e32 v209, v229
	v_add_u32_e32 v245, 0x6000, v182
	v_exp_f32_e32 v210, v230
	ds_read_b64_tr_b16 v[44:45], v245 offset:55296
	ds_read_b64_tr_b16 v[46:47], v245 offset:55808
	ds_read_b64_tr_b16 v[166:167], v182 offset:56320
	ds_read_b64_tr_b16 v[168:169], v182 offset:56832
	v_exp_f32_e32 v211, v231
	v_exp_f32_e32 v212, v232
	v_cvt_pk_bf16_f32 v36, v200, v201
	v_cvt_pk_bf16_f32 v37, v202, v203
	v_cvt_pk_bf16_f32 v38, v204, v205
	v_cvt_pk_bf16_f32 v39, v206, v207
	s_waitcnt lgkmcnt(4)
	v_mfma_f32_32x32x16_bf16 v[20:35], v[40:43], v[36:39], v[20:35]
	v_exp_f32_e32 v213, v233
	ds_read_b64_tr_b16 v[40:41], v245 offset:56320
	ds_read_b64_tr_b16 v[42:43], v245 offset:56832
	s_waitcnt lgkmcnt(4)
	v_mfma_f32_32x32x16_bf16 v[4:19], v[44:47], v[36:39], v[4:19]
	v_exp_f32_e32 v214, v234
	v_exp_f32_e32 v215, v235
	v_cvt_pk_bf16_f32 v36, v208, v209
	v_cvt_pk_bf16_f32 v37, v210, v211
	v_cvt_pk_bf16_f32 v38, v212, v213
	v_cvt_pk_bf16_f32 v39, v214, v215
	s_waitcnt lgkmcnt(2)
	v_mfma_f32_32x32x16_bf16 v[20:35], v[166:169], v[36:39], v[20:35]
	s_add_i32 s4, s4, 1
	s_waitcnt lgkmcnt(0)
	v_mfma_f32_32x32x16_bf16 v[4:19], v[40:43], v[36:39], v[4:19]
	v_pk_add_f32 v[236:237], v[200:201], v[202:203]
	v_pk_add_f32 v[238:239], v[204:205], v[206:207]
	v_pk_add_f32 v[240:241], v[208:209], v[210:211]
	v_pk_add_f32 v[242:243], v[212:213], v[214:215]
	v_pk_add_f32 v[236:237], v[236:237], v[238:239]
	v_pk_add_f32 v[240:241], v[240:241], v[242:243]
	v_pk_add_f32 v[236:237], v[236:237], v[240:241]
	v_add_f32_e32 v236, v236, v237
	v_add_f32_e32 v3, v3, v236
	v_add_u32_e32 v137, 0x800, v137
	v_add_u32_e32 v140, 0x1200, v140
	s_cmp_lt_u32 s4, 4
	v_add_u32_e32 v141, 0x80, v141
	s_cbranch_scc0 .LBB0_953
.LBB0_951:
	v_add_u32_e32 v244, 0x1a400, v141
	ds_read2_b32 v[36:37], v244 offset1:1
	ds_read2_b32 v[38:39], v244 offset0:2 offset1:3
	ds_read2_b32 v[40:41], v244 offset0:8 offset1:9
	ds_read2_b32 v[42:43], v244 offset0:10 offset1:11
	v_add_u32_e32 v174, 0, v140
	ds_read_b128 v[166:169], v174
	ds_read2_b32 v[44:45], v244 offset0:16 offset1:17
	ds_read2_b32 v[46:47], v244 offset0:18 offset1:19
	ds_read2_b32 v[48:49], v244 offset0:24 offset1:25
	ds_read2_b32 v[50:51], v244 offset0:26 offset1:27
	ds_read_b128 v[170:173], v174 offset:32
	s_waitcnt vmcnt(21) lgkmcnt(1)
	v_mfma_f32_32x32x16_bf16 v[36:51], v[166:169], v[60:63], v[36:51]
	s_waitcnt vmcnt(20) lgkmcnt(0)
	v_mfma_f32_32x32x16_bf16 v[36:51], v[170:173], v[74:77], v[36:51]
	ds_read_b128 v[166:169], v174 offset:64
	ds_read_b128 v[170:173], v174 offset:96
	s_waitcnt vmcnt(19) lgkmcnt(1)
	v_mfma_f32_32x32x16_bf16 v[36:51], v[166:169], v[78:81], v[36:51]
	s_waitcnt vmcnt(18) lgkmcnt(0)
	v_mfma_f32_32x32x16_bf16 v[36:51], v[170:173], v[82:85], v[36:51]
	s_nop 11
	v_max3_f32 v166, v36, v37, v38
	v_max3_f32 v167, v39, v40, v41
	v_max3_f32 v168, v42, v43, v44
	v_max3_f32 v169, v45, v46, v47
	v_max3_f32 v170, v48, v49, v50
	v_max3_f32 v166, v166, v167, v51
	v_max3_f32 v168, v168, v169, v170
	v_max_f32_e32 v166, v166, v168
	v_mov_b32_e32 v167, v166
	s_nop 1
	v_permlane32_swap_b32_e32 v166, v167
	v_max_f32_e32 v166, v166, v167
	v_add_f32_e32 v167, 0x41000000, v65
	v_cmp_gt_f32_e32 vcc, v166, v167
	s_cbranch_vccz .LBB0_950
	v_max_f32_e32 v166, v166, v166
	v_max_f32_e32 v167, v65, v65
	v_max_f32_e32 v167, v167, v166
	v_sub_f32_e32 v65, v65, v167
	v_exp_f32_e32 v166, v65
	v_mov_b32_e32 v65, v167
	v_pk_mul_f32 v[34:35], v[34:35], v[166:167] op_sel_hi:[1,0]
	v_pk_mul_f32 v[32:33], v[32:33], v[166:167] op_sel_hi:[1,0]
	v_pk_mul_f32 v[30:31], v[30:31], v[166:167] op_sel_hi:[1,0]
	v_pk_mul_f32 v[28:29], v[28:29], v[166:167] op_sel_hi:[1,0]
	v_pk_mul_f32 v[26:27], v[26:27], v[166:167] op_sel_hi:[1,0]
	v_pk_mul_f32 v[24:25], v[24:25], v[166:167] op_sel_hi:[1,0]
	v_pk_mul_f32 v[22:23], v[22:23], v[166:167] op_sel_hi:[1,0]
	v_pk_mul_f32 v[20:21], v[20:21], v[166:167] op_sel_hi:[1,0]
	v_pk_mul_f32 v[18:19], v[18:19], v[166:167] op_sel_hi:[1,0]
	v_pk_mul_f32 v[16:17], v[16:17], v[166:167] op_sel_hi:[1,0]
	v_pk_mul_f32 v[14:15], v[14:15], v[166:167] op_sel_hi:[1,0]
	v_pk_mul_f32 v[12:13], v[12:13], v[166:167] op_sel_hi:[1,0]
	v_pk_mul_f32 v[10:11], v[10:11], v[166:167] op_sel_hi:[1,0]
	v_pk_mul_f32 v[8:9], v[8:9], v[166:167] op_sel_hi:[1,0]
	v_pk_mul_f32 v[6:7], v[6:7], v[166:167] op_sel_hi:[1,0]
	v_pk_mul_f32 v[4:5], v[4:5], v[166:167] op_sel_hi:[1,0]
	v_mul_f32_e32 v3, v3, v166
	s_branch .LBB0_950

; #define LAS __attribute__((address_space(3)))
; template <bool BAND, int OUTMODE>
; __device__ __forceinline__ void compute(LAS unsigned char* lds, const bf16x8 (&qr)[4], int tid, int mq0, int dil, int res, int kt_min, int bias_tab, float sink2,
;                                         bf16* ob, int opitch, float* lsep) {
;     ...
;             for (int i = 0; i < 16; ++i) S[i] = bl[32 * t + (i & 3) + 8 * (i >> 2)];
;         } else {
; #pragma unroll
;             for (int i = 0; i < 16; ++i) S[i] = 0.f;
;         }
; #pragma unroll
;         for (int s = 0; s < 4; ++s) { const bf16x8 kf = *(const LAS bf16x8*)(kb + t * 32 * KSTR + s * 32); S = __builtin_amdgcn_mfma_f32_32x32x16_bf16(kf, qr[s], S, 0, 0, 0); }
;         float m0 = fmaxf(fmaxf(S[0], S[1]), fmaxf(S[2], S[3])), m1 = fmaxf(fmaxf(S[4], S[5]), fmaxf(S[6], S[7])), m2 = fmaxf(fmaxf(S[8], S[9]), fmaxf(S[10], S[11])), m3 = fmaxf(fmaxf(S[12], S[13]), fmaxf(S[14], S[15]));
;         const float mt = xhalf_max(fmaxf(fmaxf(m0, m1), fmaxf(m2, m3)));
;         if (__any(mt > mref + THR)) {
;             const float mnew = fmaxf(mref, mt), f = __builtin_amdgcn_exp2f(mref - mnew);
;             mref = mnew; l *= f;
; #pragma unroll
;             for (int i = 0; i < 16; ++i) { o0[i] *= f; o1[i] *= f; }
;         }
; #pragma unroll
;         for (int i = 0; i < 16; ++i) { const float p = __builtin_amdgcn_exp2f(S[i] - mref); S[i] = p; l += p; }
; #pragma unroll
;         for (int s = 0; s < 2; ++s) {
;             v4u pw; pw.x = cvtpk(S[8 * s + 0], S[8 * s + 1]); pw.y = cvtpk(S[8 * s + 2], S[8 * s + 3]); pw.z = cvtpk(S[8 * s + 4], S[8 * s + 5]); pw.w = cvtpk(S[8 * s + 6], S[8 * s + 7]);
;             const bf16x8 pa = __builtin_bit_cast(bf16x8, pw);
;             const LAS unsigned char* vp = vb + (32 * t + 16 * s) * 64;
;             const s16x4 a0 = vtr(vp), a1 = vtr(vp + 8 * 64), b0 = vtr(vp + VPLANE), b1 = vtr(vp + VPLANE + 8 * 64);
;             const bf16x8 v0 = __builtin_shufflevector(a0, a1, 0, 1, 2, 3, 4, 5, 6, 7), v1 = __builtin_shufflevector(b0, b1, 0, 1, 2, 3, 4, 5, 6, 7);
;             o0 = __builtin_amdgcn_mfma_f32_32x32x16_bf16(v0, pa, o0, 0, 0, 0);
;             o1 = __builtin_amdgcn_mfma_f32_32x32x16_bf16(v1, pa, o1, 0, 0, 0);
;         }
;     }
.LBB0_960:
	v_pk_add_f32 v[220:221], v[50:51], v[130:131] op_sel_hi:[1,0] neg_lo:[0,1] neg_hi:[0,1]
	v_pk_add_f32 v[222:223], v[52:53], v[130:131] op_sel_hi:[1,0] neg_lo:[0,1] neg_hi:[0,1]
	v_pk_add_f32 v[224:225], v[54:55], v[130:131] op_sel_hi:[1,0] neg_lo:[0,1] neg_hi:[0,1]
	v_pk_add_f32 v[226:227], v[56:57], v[130:131] op_sel_hi:[1,0] neg_lo:[0,1] neg_hi:[0,1]
	v_pk_add_f32 v[228:229], v[58:59], v[130:131] op_sel_hi:[1,0] neg_lo:[0,1] neg_hi:[0,1]
	v_pk_add_f32 v[230:231], v[60:61], v[130:131] op_sel_hi:[1,0] neg_lo:[0,1] neg_hi:[0,1]
	v_pk_add_f32 v[232:233], v[62:63], v[130:131] op_sel_hi:[1,0] neg_lo:[0,1] neg_hi:[0,1]
	v_pk_add_f32 v[234:235], v[64:65], v[130:131] op_sel_hi:[1,0] neg_lo:[0,1] neg_hi:[0,1]
	v_exp_f32_e32 v201, v221
	v_exp_f32_e32 v202, v222
	v_exp_f32_e32 v203, v223
	v_exp_f32_e32 v204, v224
	v_exp_f32_e32 v205, v225
	v_exp_f32_e32 v206, v226
	v_exp_f32_e32 v207, v227
	v_add_u32_e32 v137, 0, v131
	v_exp_f32_e32 v200, v220
	v_exp_f32_e32 v208, v228
	ds_read_b64_tr_b16 v[8:9], v137 offset:55296
	ds_read_b64_tr_b16 v[10:11], v137 offset:55808
	v_exp_f32_e32 v209, v229
	v_add_u32_e32 v245, 0x6000, v137
	v_exp_f32_e32 v210, v230
	ds_read_b64_tr_b16 v[12:13], v245 offset:55296
	ds_read_b64_tr_b16 v[14:15], v245 offset:55808
	ds_read_b64_tr_b16 v[50:51], v137 offset:56320
	ds_read_b64_tr_b16 v[52:53], v137 offset:56832
	v_exp_f32_e32 v211, v231
	v_exp_f32_e32 v212, v232
	v_cvt_pk_bf16_f32 v4, v200, v201
	v_cvt_pk_bf16_f32 v5, v202, v203
	v_cvt_pk_bf16_f32 v6, v204, v205
	v_cvt_pk_bf16_f32 v7, v206, v207
	s_waitcnt lgkmcnt(4)
	v_mfma_f32_32x32x16_bf16 v[34:49], v[8:11], v[4:7], v[34:49]
	v_exp_f32_e32 v213, v233
	ds_read_b64_tr_b16 v[8:9], v245 offset:56320
	ds_read_b64_tr_b16 v[10:11], v245 offset:56832
	s_waitcnt lgkmcnt(4)
	v_mfma_f32_32x32x16_bf16 v[18:33], v[12:15], v[4:7], v[18:33]
	v_exp_f32_e32 v214, v234
	v_exp_f32_e32 v215, v235
	v_cvt_pk_bf16_f32 v4, v208, v209
	v_cvt_pk_bf16_f32 v5, v210, v211
	v_cvt_pk_bf16_f32 v6, v212, v213
	v_cvt_pk_bf16_f32 v7, v214, v215
	s_waitcnt lgkmcnt(2)
	v_mfma_f32_32x32x16_bf16 v[34:49], v[50:53], v[4:7], v[34:49]
	s_add_i32 s4, s4, 1
	s_waitcnt lgkmcnt(0)
	v_mfma_f32_32x32x16_bf16 v[18:33], v[8:11], v[4:7], v[18:33]
	v_pk_add_f32 v[236:237], v[200:201], v[202:203]
	v_pk_add_f32 v[238:239], v[204:205], v[206:207]
	v_pk_add_f32 v[240:241], v[208:209], v[210:211]
	v_pk_add_f32 v[242:243], v[212:213], v[214:215]
	v_pk_add_f32 v[236:237], v[236:237], v[238:239]
	v_pk_add_f32 v[240:241], v[240:241], v[242:243]
	v_pk_add_f32 v[236:237], v[236:237], v[240:241]
	v_add_f32_e32 v236, v236, v237
	v_add_f32_e32 v3, v3, v236
	v_add_u32_e32 v131, 0x800, v131
	v_add_u32_e32 v132, 0x1200, v132
	s_cmp_lt_u32 s4, 4
	v_add_u32_e32 v133, 0x80, v133
	s_cbranch_scc0 .LBB0_963
.LBB0_961:
	v_add_u32_e32 v244, 0x1b000, v133
	ds_read2_b32 v[50:51], v244 offset1:1
	ds_read2_b32 v[52:53], v244 offset0:2 offset1:3
	ds_read2_b32 v[54:55], v244 offset0:8 offset1:9
	ds_read2_b32 v[56:57], v244 offset0:10 offset1:11
	v_add_u32_e32 v12, 0, v132
	ds_read_b128 v[4:7], v12
	ds_read2_b32 v[58:59], v244 offset0:16 offset1:17
	ds_read2_b32 v[60:61], v244 offset0:18 offset1:19
	ds_read2_b32 v[62:63], v244 offset0:24 offset1:25
	ds_read2_b32 v[64:65], v244 offset0:26 offset1:27
	ds_read_b128 v[8:11], v12 offset:32
	s_waitcnt vmcnt(17) lgkmcnt(1)
	v_mfma_f32_32x32x16_bf16 v[50:65], v[4:7], v[86:89], v[50:65]
	s_waitcnt vmcnt(16) lgkmcnt(0)
	v_mfma_f32_32x32x16_bf16 v[50:65], v[8:11], v[90:93], v[50:65]
	ds_read_b128 v[4:7], v12 offset:64
	ds_read_b128 v[8:11], v12 offset:96
	s_waitcnt vmcnt(15) lgkmcnt(1)
	v_mfma_f32_32x32x16_bf16 v[50:65], v[4:7], v[94:97], v[50:65]
	s_waitcnt vmcnt(14) lgkmcnt(0)
	v_mfma_f32_32x32x16_bf16 v[50:65], v[8:11], v[98:101], v[50:65]
	s_nop 11
	v_max3_f32 v2, v50, v51, v52
	v_max3_f32 v4, v53, v54, v55
	v_max3_f32 v5, v56, v57, v58
	v_max3_f32 v6, v59, v60, v61
	v_max3_f32 v7, v62, v63, v64
	v_max3_f32 v2, v2, v4, v65
	v_max3_f32 v5, v5, v6, v7
	v_max_f32_e32 v2, v2, v5
	v_mov_b32_e32 v4, v2
	s_nop 1
	v_permlane32_swap_b32_e32 v2, v4
	v_max_f32_e32 v2, v2, v4
	v_add_f32_e32 v4, 0x41000000, v130
	v_cmp_gt_f32_e32 vcc, v2, v4
	s_cbranch_vccz .LBB0_960
	v_max_f32_e32 v2, v2, v2
	v_max_f32_e32 v4, v130, v130
	v_max_f32_e32 v4, v4, v2
	v_sub_f32_e32 v2, v130, v4
	v_exp_f32_e32 v2, v2
	v_mov_b32_e32 v130, v4
	v_pk_mul_f32 v[48:49], v[48:49], v[2:3] op_sel_hi:[1,0]
	v_pk_mul_f32 v[46:47], v[46:47], v[2:3] op_sel_hi:[1,0]
	v_pk_mul_f32 v[44:45], v[44:45], v[2:3] op_sel_hi:[1,0]
	v_pk_mul_f32 v[42:43], v[42:43], v[2:3] op_sel_hi:[1,0]
	v_pk_mul_f32 v[40:41], v[40:41], v[2:3] op_sel_hi:[1,0]
	v_pk_mul_f32 v[38:39], v[38:39], v[2:3] op_sel_hi:[1,0]
	v_pk_mul_f32 v[36:37], v[36:37], v[2:3] op_sel_hi:[1,0]
	v_pk_mul_f32 v[34:35], v[34:35], v[2:3] op_sel_hi:[1,0]
	v_pk_mul_f32 v[32:33], v[32:33], v[2:3] op_sel_hi:[1,0]
	v_pk_mul_f32 v[30:31], v[30:31], v[2:3] op_sel_hi:[1,0]
	v_pk_mul_f32 v[28:29], v[28:29], v[2:3] op_sel_hi:[1,0]
	v_pk_mul_f32 v[26:27], v[26:27], v[2:3] op_sel_hi:[1,0]
	v_pk_mul_f32 v[24:25], v[24:25], v[2:3] op_sel_hi:[1,0]
	v_pk_mul_f32 v[22:23], v[22:23], v[2:3] op_sel_hi:[1,0]
	v_pk_mul_f32 v[20:21], v[20:21], v[2:3] op_sel_hi:[1,0]
	v_pk_mul_f32 v[18:19], v[18:19], v[2:3] op_sel_hi:[1,0]
	v_mul_f32_e32 v3, v3, v2
	s_branch .LBB0_960

; #define LAS __attribute__((address_space(3)))
; __device__ __forceinline__ unsigned cvtpk(float lo, float hi) { f32x2_t v = {lo, hi}; bf16x2_t b = __builtin_convertvector(v, bf16x2_t); return __builtin_bit_cast(unsigned, b); }
; __device__ __forceinline__ s16x4 vtr(const LAS unsigned char* p) { return __builtin_bit_cast(s16x4, __builtin_amdgcn_ds_read_tr16_b64_v4i16((LAS v4i16_t*)p)); }
; template <bool BAND, int OUTMODE>
; __device__ __forceinline__ void compute(LAS unsigned char* lds, const bf16x8 (&qr)[4], int tid, int mq0, int dil, int res, int kt_min, int bias_tab, float sink2,
;                                         bf16* ob, int opitch, float* lsep) {
;     ...
;         for (int s = 0; s < 4; ++s) { const bf16x8 kf = *(const LAS bf16x8*)(kb + t * 32 * KSTR + s * 32); S = __builtin_amdgcn_mfma_f32_32x32x16_bf16(kf, qr[s], S, 0, 0, 0); }
;         float m0 = fmaxf(fmaxf(S[0], S[1]), fmaxf(S[2], S[3])), m1 = fmaxf(fmaxf(S[4], S[5]), fmaxf(S[6], S[7])), m2 = fmaxf(fmaxf(S[8], S[9]), fmaxf(S[10], S[11])), m3 = fmaxf(fmaxf(S[12], S[13]), fmaxf(S[14], S[15]));
;         const float mt = xhalf_max(fmaxf(fmaxf(m0, m1), fmaxf(m2, m3)));
;         if (__any(mt > mref + THR)) {
;             const float mnew = fmaxf(mref, mt), f = __builtin_amdgcn_exp2f(mref - mnew);
;             mref = mnew; l *= f;
; #pragma unroll
;             for (int i = 0; i < 16; ++i) { o0[i] *= f; o1[i] *= f; }
;         }
; #pragma unroll
;         for (int i = 0; i < 16; ++i) { const float p = __builtin_amdgcn_exp2f(S[i] - mref); S[i] = p; l += p; }
; #pragma unroll
;         for (int s = 0; s < 2; ++s) {
;             v4u pw; pw.x = cvtpk(S[8 * s + 0], S[8 * s + 1]); pw.y = cvtpk(S[8 * s + 2], S[8 * s + 3]); pw.z = cvtpk(S[8 * s + 4], S[8 * s + 5]); pw.w = cvtpk(S[8 * s + 6], S[8 * s + 7]);
;             const bf16x8 pa = __builtin_bit_cast(bf16x8, pw);
;             const LAS unsigned char* vp = vb + (32 * t + 16 * s) * 64;
;             const s16x4 a0 = vtr(vp), a1 = vtr(vp + 8 * 64), b0 = vtr(vp + VPLANE), b1 = vtr(vp + VPLANE + 8 * 64);
;             const bf16x8 v0 = __builtin_shufflevector(a0, a1, 0, 1, 2, 3, 4, 5, 6, 7), v1 = __builtin_shufflevector(b0, b1, 0, 1, 2, 3, 4, 5, 6, 7);
;             o0 = __builtin_amdgcn_mfma_f32_32x32x16_bf16(v0, pa, o0, 0, 0, 0);
;             o1 = __builtin_amdgcn_mfma_f32_32x32x16_bf16(v1, pa, o1, 0, 0, 0);
;         }
.LBB0_968:
	v_pk_add_f32 v[220:221], v[36:37], v[52:53] op_sel:[0,1] op_sel_hi:[1,1] neg_lo:[0,1] neg_hi:[0,1]
	v_pk_add_f32 v[222:223], v[38:39], v[52:53] op_sel:[0,1] op_sel_hi:[1,1] neg_lo:[0,1] neg_hi:[0,1]
	v_pk_add_f32 v[224:225], v[40:41], v[52:53] op_sel:[0,1] op_sel_hi:[1,1] neg_lo:[0,1] neg_hi:[0,1]
	v_pk_add_f32 v[226:227], v[42:43], v[52:53] op_sel:[0,1] op_sel_hi:[1,1] neg_lo:[0,1] neg_hi:[0,1]
	v_pk_add_f32 v[228:229], v[44:45], v[52:53] op_sel:[0,1] op_sel_hi:[1,1] neg_lo:[0,1] neg_hi:[0,1]
	v_pk_add_f32 v[230:231], v[46:47], v[52:53] op_sel:[0,1] op_sel_hi:[1,1] neg_lo:[0,1] neg_hi:[0,1]
	v_pk_add_f32 v[232:233], v[48:49], v[52:53] op_sel:[0,1] op_sel_hi:[1,1] neg_lo:[0,1] neg_hi:[0,1]
	v_pk_add_f32 v[234:235], v[50:51], v[52:53] op_sel:[0,1] op_sel_hi:[1,1] neg_lo:[0,1] neg_hi:[0,1]
	v_exp_f32_e32 v201, v221
	v_exp_f32_e32 v202, v222
	v_exp_f32_e32 v203, v223
	v_exp_f32_e32 v204, v224
	v_exp_f32_e32 v205, v225
	v_exp_f32_e32 v206, v226
	v_exp_f32_e32 v207, v227
	v_add_u32_e32 v69, v1, v134
	v_exp_f32_e32 v200, v220
	v_exp_f32_e32 v208, v228
	ds_read_b64_tr_b16 v[40:41], v69 offset:55296
	ds_read_b64_tr_b16 v[42:43], v69 offset:55808
	v_exp_f32_e32 v209, v229
	v_add_u32_e32 v245, 0x6000, v69
	v_exp_f32_e32 v210, v230
	ds_read_b64_tr_b16 v[44:45], v245 offset:55296
	ds_read_b64_tr_b16 v[46:47], v245 offset:55808
	ds_read_b64_tr_b16 v[54:55], v69 offset:56320
	ds_read_b64_tr_b16 v[56:57], v69 offset:56832
	v_exp_f32_e32 v211, v231
	v_exp_f32_e32 v212, v232
	v_cvt_pk_bf16_f32 v36, v200, v201
	v_cvt_pk_bf16_f32 v37, v202, v203
	v_cvt_pk_bf16_f32 v38, v204, v205
	v_cvt_pk_bf16_f32 v39, v206, v207
	s_waitcnt lgkmcnt(4)
	v_mfma_f32_32x32x16_bf16 v[18:33], v[40:43], v[36:39], v[18:33]
	v_exp_f32_e32 v213, v233
	ds_read_b64_tr_b16 v[40:41], v245 offset:56320
	ds_read_b64_tr_b16 v[42:43], v245 offset:56832
	s_waitcnt lgkmcnt(4)
	v_mfma_f32_32x32x16_bf16 v[2:17], v[44:47], v[36:39], v[2:17]
	v_exp_f32_e32 v214, v234
	v_exp_f32_e32 v215, v235
	v_cvt_pk_bf16_f32 v36, v208, v209
	v_cvt_pk_bf16_f32 v37, v210, v211
	v_cvt_pk_bf16_f32 v38, v212, v213
	v_cvt_pk_bf16_f32 v39, v214, v215
	s_waitcnt lgkmcnt(2)
	v_mfma_f32_32x32x16_bf16 v[18:33], v[54:57], v[36:39], v[18:33]
	s_add_i32 s3, s3, -1
	s_waitcnt lgkmcnt(0)
	v_mfma_f32_32x32x16_bf16 v[2:17], v[40:43], v[36:39], v[2:17]
	v_pk_add_f32 v[236:237], v[200:201], v[202:203]
	v_pk_add_f32 v[238:239], v[204:205], v[206:207]
	v_pk_add_f32 v[240:241], v[208:209], v[210:211]
	v_pk_add_f32 v[242:243], v[212:213], v[214:215]
	v_pk_add_f32 v[236:237], v[236:237], v[238:239]
	v_pk_add_f32 v[240:241], v[240:241], v[242:243]
	v_pk_add_f32 v[236:237], v[236:237], v[240:241]
	v_add_f32_e32 v236, v236, v237
	v_add_f32_e32 v34, v34, v236
	v_add_u32_e32 v1, 0x800, v1
	s_cmp_lg_u32 s3, 0
	v_add_u32_e32 v52, 0x1200, v52
	s_cbranch_scc0 .LBB0_971
